# expert GEMM phases: dead per-XCD max-round computation removed; dispatch phase: 16 histogram loads per thread issued together
# baseline (speedup 1.0000x reference)
; DI void p_dispatch(Frame& F) {
;     ...
;     for (int blk = F.bx; blk < T / 128; blk += F.G) {
;         { const int e = F.tid & 31, part = F.tid >> 5; int tot = 0, bs = 0;
;           for (int b2 = part * 16; b2 < part * 16 + 16; ++b2) { const int c = hist[b2 * 32 + e]; tot += c; bs += (b2 < blk) ? c : 0; }
;           PT[part * 32 + e] = tot; PB[part * 32 + e] = bs; }
;         __syncthreads();
;         if (F.tid < 32) { int tot = 0, bs = 0;
;             for (int p = 0; p < 16; ++p) { tot += PT[p * 32 + F.tid]; bs += PB[p * 32 + F.tid]; }
;             PT[F.tid] = (tot + 255) >> 8; BASE[F.tid] = bs; TOT[F.tid] = tot; }
.LBB0_3436:
	v_lshlrev_b32_e32 v151, 7, v4
	v_lshl_add_u32 v151, v2, 2, v151
	global_load_dword v152, v151, s[14:15]
	global_load_dword v153, v151, s[14:15] offset:128
	global_load_dword v154, v151, s[14:15] offset:256
	global_load_dword v155, v151, s[14:15] offset:384
	global_load_dword v156, v151, s[14:15] offset:512
	global_load_dword v157, v151, s[14:15] offset:640
	global_load_dword v158, v151, s[14:15] offset:768
	global_load_dword v159, v151, s[14:15] offset:896
	global_load_dword v160, v151, s[14:15] offset:1024
	global_load_dword v161, v151, s[14:15] offset:1152
	global_load_dword v162, v151, s[14:15] offset:1280
	global_load_dword v163, v151, s[14:15] offset:1408
	global_load_dword v164, v151, s[14:15] offset:1536
	global_load_dword v165, v151, s[14:15] offset:1664
	global_load_dword v166, v151, s[14:15] offset:1792
	global_load_dword v167, v151, s[14:15] offset:1920
	v_sub_u32_e32 v168, s30, v4
	v_mov_b32_e32 v17, 0
	v_mov_b32_e32 v16, 0
	s_waitcnt vmcnt(0)
	v_cmp_lt_i32_e64 s[26:27], 0, v168
	v_add_u32_e32 v17, v17, v152
	s_nop 1
	v_cndmask_b32_e64 v0, 0, v152, s[26:27]
	v_add_u32_e32 v16, v16, v0
	v_cmp_lt_i32_e64 s[26:27], 1, v168
	v_add_u32_e32 v17, v17, v153
	s_nop 1
	v_cndmask_b32_e64 v0, 0, v153, s[26:27]
	v_add_u32_e32 v16, v16, v0
	v_cmp_lt_i32_e64 s[26:27], 2, v168
	v_add_u32_e32 v17, v17, v154
	s_nop 1
	v_cndmask_b32_e64 v0, 0, v154, s[26:27]
	v_add_u32_e32 v16, v16, v0
	v_cmp_lt_i32_e64 s[26:27], 3, v168
	v_add_u32_e32 v17, v17, v155
	s_nop 1
	v_cndmask_b32_e64 v0, 0, v155, s[26:27]
	v_add_u32_e32 v16, v16, v0
	v_cmp_lt_i32_e64 s[26:27], 4, v168
	v_add_u32_e32 v17, v17, v156
	s_nop 1
	v_cndmask_b32_e64 v0, 0, v156, s[26:27]
	v_add_u32_e32 v16, v16, v0
	v_cmp_lt_i32_e64 s[26:27], 5, v168
	v_add_u32_e32 v17, v17, v157
	s_nop 1
	v_cndmask_b32_e64 v0, 0, v157, s[26:27]
	v_add_u32_e32 v16, v16, v0
	v_cmp_lt_i32_e64 s[26:27], 6, v168
	v_add_u32_e32 v17, v17, v158
	s_nop 1
	v_cndmask_b32_e64 v0, 0, v158, s[26:27]
	v_add_u32_e32 v16, v16, v0
	v_cmp_lt_i32_e64 s[26:27], 7, v168
	v_add_u32_e32 v17, v17, v159
	s_nop 1
	v_cndmask_b32_e64 v0, 0, v159, s[26:27]
	v_add_u32_e32 v16, v16, v0
	v_cmp_lt_i32_e64 s[26:27], 8, v168
	v_add_u32_e32 v17, v17, v160
	s_nop 1
	v_cndmask_b32_e64 v0, 0, v160, s[26:27]
	v_add_u32_e32 v16, v16, v0
	v_cmp_lt_i32_e64 s[26:27], 9, v168
	v_add_u32_e32 v17, v17, v161
	s_nop 1
	v_cndmask_b32_e64 v0, 0, v161, s[26:27]
	v_add_u32_e32 v16, v16, v0
	v_cmp_lt_i32_e64 s[26:27], 10, v168
	v_add_u32_e32 v17, v17, v162
	s_nop 1
	v_cndmask_b32_e64 v0, 0, v162, s[26:27]
	v_add_u32_e32 v16, v16, v0
	v_cmp_lt_i32_e64 s[26:27], 11, v168
	v_add_u32_e32 v17, v17, v163
	s_nop 1
	v_cndmask_b32_e64 v0, 0, v163, s[26:27]
	v_add_u32_e32 v16, v16, v0
	v_cmp_lt_i32_e64 s[26:27], 12, v168
	v_add_u32_e32 v17, v17, v164
	s_nop 1
	v_cndmask_b32_e64 v0, 0, v164, s[26:27]
	v_add_u32_e32 v16, v16, v0
	v_cmp_lt_i32_e64 s[26:27], 13, v168
	v_add_u32_e32 v17, v17, v165
	s_nop 1
	v_cndmask_b32_e64 v0, 0, v165, s[26:27]
	v_add_u32_e32 v16, v16, v0
	v_cmp_lt_i32_e64 s[26:27], 14, v168
	v_add_u32_e32 v17, v17, v166
	s_nop 1
	v_cndmask_b32_e64 v0, 0, v166, s[26:27]
	v_add_u32_e32 v16, v16, v0
	v_cmp_lt_i32_e64 s[26:27], 15, v168
	v_add_u32_e32 v17, v17, v167
	s_nop 1
	v_cndmask_b32_e64 v0, 0, v167, s[26:27]
	v_add_u32_e32 v16, v16, v0
	ds_write2st64_b32 v11, v17, v16 offset1:8
	s_waitcnt lgkmcnt(0)
	s_barrier
	s_and_saveexec_b64 s[0:1], vcc
	s_cbranch_execz .LBB0_3446
	v_add_u32_e32 v0, 0x800, v11
	ds_read2_b32 v[8:9], v11 offset1:32
	ds_read2_b32 v[16:17], v0 offset1:32
	v_add_u32_e32 v20, 0xc00, v11
	s_waitcnt lgkmcnt(1)
	v_add_u32_e32 v18, v9, v8
	s_waitcnt lgkmcnt(0)
	v_add_u32_e32 v19, v17, v16
	ds_read2_b32 v[8:9], v11 offset0:64 offset1:96
	ds_read2_b32 v[16:17], v0 offset0:64 offset1:96
	s_waitcnt lgkmcnt(1)
	v_add3_u32 v18, v18, v8, v9
	s_waitcnt lgkmcnt(0)
	v_add3_u32 v19, v19, v16, v17
	ds_read2_b32 v[8:9], v11 offset0:128 offset1:160
	ds_read2_b32 v[16:17], v0 offset0:128 offset1:160
	s_waitcnt lgkmcnt(1)
	v_add3_u32 v18, v18, v8, v9
	s_waitcnt lgkmcnt(0)
	v_add3_u32 v19, v19, v16, v17
	ds_read2_b32 v[8:9], v11 offset0:192 offset1:224
	ds_read2_b32 v[16:17], v0 offset0:192 offset1:224
	s_waitcnt lgkmcnt(1)
	v_add3_u32 v0, v18, v8, v9
	s_waitcnt lgkmcnt(0)
	v_add3_u32 v18, v19, v16, v17
	v_add_u32_e32 v19, 0x400, v11
	ds_read2_b32 v[8:9], v19 offset1:32
	ds_read2_b32 v[16:17], v20 offset1:32
	s_waitcnt lgkmcnt(1)
	v_add3_u32 v0, v0, v8, v9
	s_waitcnt lgkmcnt(0)
	v_add3_u32 v18, v18, v16, v17
	ds_read2_b32 v[8:9], v19 offset0:64 offset1:96
	ds_read2_b32 v[16:17], v20 offset0:64 offset1:96
	s_waitcnt lgkmcnt(1)
	v_add3_u32 v0, v0, v8, v9
	s_waitcnt lgkmcnt(0)
	v_add3_u32 v18, v18, v16, v17
	ds_read2_b32 v[8:9], v19 offset0:128 offset1:160
	ds_read2_b32 v[16:17], v20 offset0:128 offset1:160
	s_waitcnt lgkmcnt(1)
	v_add3_u32 v0, v0, v8, v9
	s_waitcnt lgkmcnt(0)
	v_add3_u32 v18, v18, v16, v17
	ds_read2_b32 v[8:9], v19 offset0:192 offset1:224
	ds_read2_b32 v[16:17], v20 offset0:192 offset1:224
	s_waitcnt lgkmcnt(1)
	v_add3_u32 v0, v0, v8, v9
	v_add_u32_e32 v9, 0xff, v0
	s_waitcnt lgkmcnt(0)
	v_add3_u32 v8, v18, v16, v17
	v_ashrrev_i32_e32 v9, 8, v9
	ds_write2st64_b32 v11, v9, v8 offset1:17
	ds_write_b32 v11, v0 offset:4480

; #define LAS __attribute__((address_space(3)))
; __global__ void __launch_bounds__(NWAVES * 64, 2) mega_fwd(Args args) {
;     ...
;             if (F.tid == 0) { int run = 0; for (int s_ = 0; s_ < 4; ++s_) { const int e_ = (F.bx & 7) + 8 * s_; TS[40 + s_] = run; TS[48 + s_] = TS[e_]; run += 4 * (TS[e_ + 1] - TS[e_]); } TS[44] = run;
;                 int gm_ = 0; for (int x_ = 0; x_ < 8; ++x_) { int u_ = 0; for (int s_ = 0; s_ < 4; ++s_) u_ += 4 * (TS[x_ + 8 * s_ + 1] - TS[x_ + 8 * s_]); const int r_ = (u_ + (F.G >> 3) - 1) / (F.G >> 3); gm_ = r_ > gm_ ? r_ : gm_; } TS[45] = gm_; }
;             __syncthreads();
;             pg8::Gemm g{H, (const bf16*)(F.ws + WS_WGU + (size_t)(F.l & 1) * EXP_ALT), MOE_ROWS, NEXP * 1024, D};
;             pg8::MoeOrder S{F.G, F.bx, TS + 40};
;             LAS int* RT = (LAS int*)(F.lds + RING_BYTES + 4096);
;             { pg8::Unit u_; const int* rowtok = (const int*)(F.ws + WS_SMALL + 512 * 1024);
;               const int nxu_ = __builtin_amdgcn_readfirstlane(TS[44]), lcu_ = F.bx >> 3, peru_ = F.G >> 3; int nu_ = nxu_ > lcu_ ? (nxu_ - lcu_ + peru_ - 1) / peru_ : 0; nu_ = nu_ > 12 ? 12 : nu_;
.LBB0_3511:
	s_or_b64 exec, exec, s[0:1]
	v_cmp_eq_u32_e32 vcc, 0, v132
	s_waitcnt vmcnt(0) lgkmcnt(0)
	s_barrier
	s_and_saveexec_b64 s[0:1], vcc
	s_cbranch_execz .LBB0_3513
	s_and_b32 s4, s12, 7
	s_lshl_b32 s4, s4, 2
	s_add_i32 s4, s5, s4
	s_add_i32 s10, s30, 0x204a0
	v_mov_b32_e32 v0, s10
	v_mov_b32_e32 v2, s4
	ds_write_b32 v0, v3
	ds_read2_b32 v[0:1], v2 offset1:1
	ds_read2_b32 v[4:5], v2 offset0:8 offset1:9
	s_add_i32 s10, s30, 0x204c0
	v_mov_b32_e32 v6, s10
	s_add_i32 s4, s30, 0x204a4
	s_waitcnt lgkmcnt(1)
	v_sub_u32_e32 v1, v1, v0
	s_waitcnt lgkmcnt(0)
	ds_write2_b32 v6, v0, v4 offset1:1
	v_sub_u32_e32 v0, v5, v4
	v_add_u32_e32 v6, v0, v1
	v_lshlrev_b32_e32 v0, 2, v6
	v_lshlrev_b32_e32 v1, 2, v1
	v_mov_b32_e32 v4, s4
	ds_write2_b32 v4, v1, v0 offset1:1
	ds_read2_b32 v[0:1], v2 offset0:16 offset1:17
	ds_read2_b32 v[4:5], v2 offset0:24 offset1:25
	s_add_i32 s4, s30, 0x204c8
	v_mov_b32_e32 v2, s4
	s_add_i32 s10, s30, 0x204ac
	s_waitcnt lgkmcnt(1)
	v_sub_u32_e32 v1, v1, v0
	s_waitcnt lgkmcnt(0)
	ds_write2_b32 v2, v0, v4 offset1:1
	v_sub_u32_e32 v0, v5, v4
	v_add_u32_e32 v1, v1, v6
	v_add_u32_e32 v0, v0, v1
	v_lshlrev_b32_e32 v1, 2, v1
	v_lshlrev_b32_e32 v0, 2, v0
	v_mov_b32_e32 v2, s10
	ds_write2_b32 v2, v1, v0 offset1:1
.LBB0_3513:
	s_or_b64 exec, exec, s[0:1]
	s_add_i32 s35, s30, 0x204b0
	v_mov_b32_e32 v0, s35
	s_waitcnt lgkmcnt(0)
	s_barrier
	ds_read_b32 v0, v0
	s_ashr_i32 s36, s12, 3
	s_mov_b32 s13, 0
	s_waitcnt lgkmcnt(0)
	v_readfirstlane_b32 s0, v0
	s_cmp_le_i32 s0, s36
	s_cbranch_scc1 .LBB0_3515
	s_ashr_i32 s1, s28, 3
	s_abs_i32 s4, s1
	v_cvt_f32_u32_e32 v0, s4
	s_not_b32 s5, s36
	s_add_i32 s5, s1, s5
	s_add_i32 s5, s5, s0
	v_rcp_iflag_f32_e32 v0, v0
	s_sub_i32 s0, 0, s4
	s_xor_b32 s1, s5, s1
	s_abs_i32 s5, s5
	v_mul_f32_e32 v0, 0x4f7ffffe, v0
	v_cvt_u32_f32_e32 v0, v0
	s_ashr_i32 s1, s1, 31
	v_readfirstlane_b32 s10, v0
	s_mul_i32 s0, s0, s10
	s_mul_hi_u32 s0, s10, s0
	s_add_i32 s10, s10, s0
	s_mul_hi_u32 s0, s5, s10
	s_mul_i32 s10, s0, s4
	s_sub_i32 s5, s5, s10
	s_add_i32 s11, s0, 1
	s_sub_i32 s10, s5, s4
	s_cmp_ge_u32 s5, s4
	s_cselect_b32 s0, s11, s0
	s_cselect_b32 s5, s10, s5
	s_add_i32 s10, s0, 1
	s_cmp_ge_u32 s5, s4
	s_cselect_b32 s0, s10, s0
	s_xor_b32 s0, s0, s1
	s_sub_i32 s0, s0, s1
	s_min_i32 s13, s0, 12

;     __device__ __forceinline__ bool next(int i, Unit& u) const { return i == 0 && so.next(round, u); }
; template <class Epi, class Sched, bool ALIGN_EPI = false, bool SP2 = false, bool GATHER = false>
; __device__ __forceinline__ void gemm_phase(PG8_LAS unsigned char* lds, const Gemm g, const Sched& S, const Epi& E, const PG8_LAS int* rt = nullptr) {
;     ...
;     const int tid = tid_, wid = __builtin_amdgcn_readfirstlane(tid >> 6), lane = tid & 63, wr = wid >> 2, wc = wid & 3, fr = lane & 15, fq = lane >> 4;
;     const int K = g.K, nt = K / BK;
;     unsigned voffA[2], voffB[2];
; #pragma unroll
;     for (int i = 0; i < 2; ++i) { int R, C; stage_rc(tid * 16 + i * 8192, R, C); const int Rb = Epi::PERM ? ((R & ~31) + perm32(R & 31)) : R;
;         voffA[i] = (unsigned)(R * K + C) * 2u; voffB[i] = (unsigned)(Rb * K + C) * 2u; }
;     const size_t kstep = (size_t)(BK * 2);
;     static_assert(!GATHER || SP2, "gather needs the SP2 loop");
;     ...
;     const size_t hstep = (size_t)HALF * K * 2;
;     const size_t tstep = 2 * hstep;
;     const unsigned ldsw = (unsigned)wid * 1024u;
;     const int aoff = lds_byte(wr * 64 + fr, fq * 8), boff = lds_byte(wc * 32 + fr, fq * 8);
;     ...
;     Unit cur, nxt;
;     if (!S.next(0, cur)) return;
;     f32x4 acc[2][2][4][2];
; #pragma unroll
;     for (int a = 0; a < 2; ++a)
; #pragma unroll
;         for (int b = 0; b < 2; ++b)
; #pragma unroll
;             for (int m = 0; m < 4; ++m)
; #pragma unroll
;                 for (int n = 0; n < 2; ++n) acc[a][b][m][n] = (f32x4){0.f, 0.f, 0.f, 0.f};
;     bf16x8 At[4][2], B0[2][2], B1[2][2];
;     const char* cA = (const char*)g.A + (GATHER ? (size_t)0 : (size_t)cur.pm * tstep); const char* cB = (const char*)g.Bt + (size_t)cur.pn * tstep;
;     ...
;     bool has_next_ = false; int ui = 0;
;     S.a_ready(cur);
;     if constexpr (SP2) {
; __global__ void __launch_bounds__(NWAVES * 64, 2) mega_fwd(Args args) {
;     ...
;             if (F.tid == 0) { int run = 0; for (int s_ = 0; s_ < 4; ++s_) { const int e_ = (F.bx & 7) + 8 * s_; TS[40 + s_] = run; TS[48 + s_] = TS[e_]; run += 4 * (TS[e_ + 1] - TS[e_]); } TS[44] = run;
;                 int gm_ = 0; for (int x_ = 0; x_ < 8; ++x_) { int u_ = 0; for (int s_ = 0; s_ < 4; ++s_) u_ += 4 * (TS[x_ + 8 * s_ + 1] - TS[x_ + 8 * s_]); const int r_ = (u_ + (F.G >> 3) - 1) / (F.G >> 3); gm_ = r_ > gm_ ? r_ : gm_; } TS[45] = gm_; }
.LBB0_3860:
	s_or_b64 exec, exec, s[2:3]
	v_cmp_eq_u32_e32 vcc, 0, v4
	s_waitcnt vmcnt(0) lgkmcnt(0)
	s_barrier
	s_and_saveexec_b64 s[2:3], vcc
	s_cbranch_execz .LBB0_3862
	s_and_b32 s10, s6, 7
	s_lshl_b32 s10, s10, 2
	s_add_i32 s10, s11, s10
	s_add_i32 s12, s8, 0x204a0
	v_mov_b32_e32 v0, s12
	v_mov_b32_e32 v2, s10
	ds_write_b32 v0, v3
	ds_read2_b32 v[0:1], v2 offset1:1
	ds_read2_b32 v[4:5], v2 offset0:8 offset1:9
	s_add_i32 s12, s8, 0x204c0
	v_mov_b32_e32 v6, s12
	s_add_i32 s10, s8, 0x204a4
	s_waitcnt lgkmcnt(1)
	v_sub_u32_e32 v1, v1, v0
	s_waitcnt lgkmcnt(0)
	ds_write2_b32 v6, v0, v4 offset1:1
	v_sub_u32_e32 v0, v5, v4
	v_add_u32_e32 v6, v0, v1
	v_lshlrev_b32_e32 v0, 2, v6
	v_lshlrev_b32_e32 v1, 2, v1
	v_mov_b32_e32 v4, s10
	ds_write2_b32 v4, v1, v0 offset1:1
	ds_read2_b32 v[0:1], v2 offset0:16 offset1:17
	ds_read2_b32 v[4:5], v2 offset0:24 offset1:25
	s_add_i32 s10, s8, 0x204c8
	v_mov_b32_e32 v2, s10
	s_add_i32 s12, s8, 0x204ac
	s_waitcnt lgkmcnt(1)
	v_sub_u32_e32 v1, v1, v0
	s_waitcnt lgkmcnt(0)
	ds_write2_b32 v2, v0, v4 offset1:1
	v_sub_u32_e32 v0, v5, v4
	v_add_u32_e32 v1, v1, v6
	v_add_u32_e32 v0, v0, v1
	v_lshlrev_b32_e32 v1, 2, v1
	v_lshlrev_b32_e32 v0, 2, v0
	v_mov_b32_e32 v2, s12
	ds_write2_b32 v2, v1, v0 offset1:1
.LBB0_3862:
	s_or_b64 exec, exec, s[2:3]
	s_add_i32 s26, s8, 0x204b0
	v_mov_b32_e32 v16, v228
	v_mov_b32_e32 v0, s26
	s_waitcnt lgkmcnt(0)
	s_barrier
	ds_read_b32 v0, v0
	s_ashr_i32 s27, s6, 3
	v_readfirstlane_b32 s10, v16
	s_waitcnt lgkmcnt(0)
	v_cmp_ge_i32_e32 vcc, s27, v0
	s_cbranch_vccnz .LBB0_3878
	v_lshlrev_b32_e32 v0, 4, v16
	v_add_u32_e32 v1, 0x2000, v0
	v_ashrrev_i32_e32 v2, 31, v1
	v_lshrrev_b32_e32 v2, 22, v2
	v_add_u32_e32 v2, v1, v2
	v_ashrrev_i32_e32 v2, 10, v2
	v_mul_i32_i24_e32 v4, 0x400, v2
	v_sub_u32_e32 v1, v1, v4
	v_lshrrev_b32_e32 v4, 4, v1
	s_add_u32 s28, s4, 0x2cf00000
	v_bitop3_b32 v1, v4, v1, 32 bitop3:0x6c
	s_addc_u32 s29, s5, 0
	v_ashrrev_i32_e32 v4, 31, v1
	s_bitcmp1_b32 s7, 0
	v_lshrrev_b32_e32 v4, 26, v4
	s_cselect_b32 s2, 0x22e00000, 0
	v_add_u32_e32 v4, v1, v4
	v_lshlrev_b32_e32 v5, 3, v2
	s_add_u32 s2, s4, s2
	v_ashrrev_i32_e32 v12, 6, v4
	v_and_b32_e32 v5, -16, v5
	s_addc_u32 s3, s5, 0
	v_add_u32_e32 v5, v12, v5
	s_add_u32 s30, s2, 0x5100000
	v_and_b32_e32 v6, 3, v12
	s_mov_b32 s2, 0x3fffe0
	v_lshrrev_b32_e32 v7, 2, v5
	v_lshlrev_b32_e32 v8, 1, v5
	v_and_or_b32 v6, v5, s2, v6
	v_and_b32_e32 v7, 4, v7
	v_and_b32_e32 v8, 24, v8
	v_and_b32_e32 v4, 0xc0, v4
	v_or3_b32 v6, v6, v7, v8
	v_sub_u32_e32 v1, v1, v4
	v_mov_b32_e32 v8, 1
	v_lshlrev_b32_e32 v7, 5, v2
	v_ashrrev_i16_sdwa v1, v8, sext(v1) dst_sel:DWORD dst_unused:UNUSED_PAD src0_sel:DWORD src1_sel:BYTE_0
	v_and_b32_e32 v7, 32, v7
	v_bfe_i32 v13, v1, 0, 16
	v_add_lshl_u32 v1, v7, v13, 1
	v_lshl_add_u32 v132, v6, 10, v1
	v_lshl_add_u32 v134, v5, 10, v1
	v_bfe_i32 v1, v16, 27, 1
	v_lshrrev_b32_e32 v1, 22, v1
	v_add_u32_e32 v1, v0, v1
	v_and_b32_e32 v1, 0xfffffc00, v1
	v_sub_u32_e32 v0, v0, v1
	v_lshrrev_b32_e32 v1, 4, v0
	v_ashrrev_i32_e32 v4, 31, v16
	v_bitop3_b32 v0, v1, v0, 32 bitop3:0x6c
	v_lshrrev_b32_e32 v4, 26, v4
	v_ashrrev_i32_e32 v1, 31, v0
	v_add_u32_e32 v4, v16, v4
	v_lshrrev_b32_e32 v1, 26, v1
	v_ashrrev_i32_e32 v15, 6, v4
	v_add_u32_e32 v1, v0, v1
	v_lshlrev_b32_e32 v4, 3, v15
	v_ashrrev_i32_e32 v14, 6, v1
	v_and_b32_e32 v4, -16, v4
	v_add_u32_e32 v4, v14, v4
	v_and_b32_e32 v5, 3, v14
	v_lshrrev_b32_e32 v6, 2, v4
	v_lshlrev_b32_e32 v7, 1, v4
	v_and_or_b32 v5, v4, s2, v5
	v_and_b32_e32 v6, 4, v6
	v_and_b32_e32 v7, 24, v7
	v_and_b32_e32 v1, 0xc0, v1
	s_addc_u32 s31, s3, 0
	v_or3_b32 v5, v5, v6, v7
	v_sub_u32_e32 v7, v0, v1
	s_add_i32 s35, s8, 0x204a4
	s_add_i32 s36, s8, 0x204ac
	v_mov_b32_e32 v0, s35
	v_ashrrev_i16_sdwa v7, v8, sext(v7) dst_sel:DWORD dst_unused:UNUSED_PAD src0_sel:DWORD src1_sel:BYTE_0
	v_mov_b32_e32 v8, s36
	ds_read2_b32 v[0:1], v0 offset1:1
	ds_read_b32 v8, v8
	s_ashr_i32 s11, s10, 6
	s_add_i32 s34, s8, 0x204a0
	s_ashr_i32 s12, s10, 8
	s_lshl_b32 s7, s11, 10
	s_waitcnt lgkmcnt(1)
	v_cmp_ge_i32_e32 vcc, s27, v0
	s_waitcnt lgkmcnt(0)
	v_readfirstlane_b32 s2, v8
	s_cmp_ge_i32 s27, s2
	v_cndmask_b32_e64 v0, 0, 1, vcc
	v_cmp_ge_i32_e32 vcc, s27, v1
	s_cselect_b64 s[2:3], -1, 0
	v_readfirstlane_b32 s14, v0
	v_cndmask_b32_e64 v1, 0, 1, vcc
	s_cmp_lg_u64 s[2:3], 0
	v_readfirstlane_b32 s13, v1
	s_addc_u32 s2, s13, s14
	s_lshl_b32 s3, s2, 2
	s_add_i32 s3, s34, s3
	v_mov_b32_e32 v0, s3
	ds_read2_b32 v[0:1], v0 offset1:8
	s_lshl_b32 s2, s2, 5
	s_lshl_b32 s6, s6, 2
	s_and_b32 s37, s6, 28
	v_lshlrev_b32_e32 v6, 5, v15
	s_waitcnt lgkmcnt(0)
	v_readfirstlane_b32 s3, v0
	s_sub_i32 s3, s27, s3
	s_ashr_i32 s13, s3, 2
	v_readfirstlane_b32 s14, v1
	s_and_b32 s3, s3, 3
	s_add_i32 s18, s13, s14
	s_or_b32 s2, s2, s3
	s_or_b32 s63, s2, s37
	s_ashr_i32 s19, s18, 31
	s_lshl_b64 s[2:3], s[18:19], 18
	s_lshl_b32 s6, s63, 18
	s_add_u32 s22, s30, s6
	s_addc_u32 s23, s31, 0
	s_add_i32 s19, s8, 0x10000
	s_add_i32 s38, s19, s7
	s_add_i32 s39, s38, 0x2000
	s_add_u32 s14, s22, 0x20000
	v_and_b32_e32 v6, 32, v6
	v_bfe_i32 v17, v7, 0, 16
	s_addc_u32 s15, s23, 0
	s_add_i32 s40, s8, 0x14000
	v_add_lshl_u32 v6, v6, v17, 1
	s_add_i32 s41, s40, s7
	v_lshl_add_u32 v136, v5, 10, v6
	s_mov_b32 m0, s38
	s_add_i32 s42, s41, 0x2000
	global_load_lds_dwordx4 v136, s[22:23]
	s_mov_b32 m0, s39
	s_add_u32 s20, s28, s2
	global_load_lds_dwordx4 v132, s[22:23]
	s_mov_b32 m0, s41
	s_addc_u32 s21, s29, s3
	s_add_i32 s43, s8, s7
	global_load_lds_dwordx4 v136, s[14:15]
	s_mov_b32 m0, s42
	s_add_i32 s44, s43, 0x2000
	v_lshl_add_u32 v138, v4, 10, v6
	global_load_lds_dwordx4 v132, s[14:15]
	s_mov_b32 m0, s43
	s_add_u32 s2, s20, 0x20000
	global_load_lds_dwordx4 v138, s[20:21]
	s_mov_b32 m0, s44
	s_addc_u32 s3, s21, 0
	s_add_i32 s45, s43, 0x4000
	global_load_lds_dwordx4 v134, s[20:21]
	s_mov_b32 m0, s45
	s_add_i32 s46, s43, 0x6000
	global_load_lds_dwordx4 v138, s[2:3]
	s_mov_b32 m0, s46
	v_mov_b32_e32 v137, v3
	global_load_lds_dwordx4 v134, s[2:3]
	v_mov_b32_e32 v133, v3
	v_mov_b32_e32 v139, v3
	v_mov_b32_e32 v135, v3
	s_cmp_eq_u32 s12, 1
	v_lshl_add_u64 v[10:11], s[22:23], 0, v[136:137]
	v_lshl_add_u64 v[8:9], s[22:23], 0, v[132:133]
	v_lshl_add_u64 v[4:5], s[20:21], 0, v[138:139]
	s_cselect_b64 s[2:3], -1, 0
	s_cmp_lg_u32 s12, 1
	v_lshl_add_u64 v[6:7], s[20:21], 0, v[134:135]
	s_cbranch_scc1 .LBB0_3865
	s_barrier
